# grid-barrier and queue spin loops poll less often (s_sleep 3 instead of 1) to cut polling traffic while stragglers finish
# speedup vs baseline: 1.0017x; 1.0017x over previous
; __device__ __forceinline__ unsigned xb_ld(unsigned* p)              { return __hip_atomic_load(p, __ATOMIC_RELAXED, __HIP_MEMORY_SCOPE_AGENT); }
; __device__ __forceinline__ void xcd_barrier_complete(unsigned* bar, unsigned x, unsigned& nloc, unsigned& nx) {
;     const unsigned G = gridDim.x * gridDim.y * gridDim.z;
;     unsigned sum, cnt, mine, sp = 0u;
;     for (;;) {
;         sum = 0u; cnt = 0u; mine = 0u;
; #pragma unroll
;         for (unsigned j = 0; j < 16; ++j) { const unsigned c = xb_ld(&bar[XB_XCNT(j)]); sum += c; cnt += (c > 0u) ? 1u : 0u; mine = (j == x) ? c : mine; }
;         if (sum == G) break;
;         __builtin_amdgcn_s_sleep(1);
;         if ((++sp & 255u) == 0u) { if (xb_ld(&bar[XB_TMO])) break; if (sp > XB_SPIN_CAP) { atomicAdd(&bar[XB_TMO], 1u); break; } }
;     }
.LBB0_113:
	global_load_dword v15, v16, s[10:11] sc1
	global_load_dword v0, v16, s[12:13] sc1
	global_load_dword v1, v16, s[14:15] sc1
	global_load_dword v2, v16, s[16:17] sc1
	global_load_dword v3, v16, s[18:19] sc1
	global_load_dword v4, v16, s[20:21] sc1
	global_load_dword v5, v16, s[22:23] sc1
	global_load_dword v6, v16, s[24:25] sc1
	global_load_dword v7, v16, s[26:27] sc1
	global_load_dword v8, v16, s[28:29] sc1
	global_load_dword v9, v16, s[30:31] sc1
	global_load_dword v10, v16, s[34:35] sc1
	global_load_dword v11, v16, s[36:37] sc1
	global_load_dword v12, v16, s[38:39] sc1
	global_load_dword v13, v16, s[40:41] sc1
	global_load_dword v14, v16, s[42:43] sc1
	s_mov_b64 s[44:45], -1
	s_mov_b64 s[46:47], -1
	s_waitcnt vmcnt(14)
	v_add_u32_e32 v17, v0, v15
	s_waitcnt vmcnt(13)
	v_add_u32_e32 v17, v17, v1
	s_waitcnt vmcnt(12)
	v_add_u32_e32 v17, v17, v2
	s_waitcnt vmcnt(11)
	v_add_u32_e32 v17, v17, v3
	s_waitcnt vmcnt(10)
	v_add_u32_e32 v17, v17, v4
	s_waitcnt vmcnt(9)
	v_add_u32_e32 v17, v17, v5
	s_waitcnt vmcnt(8)
	v_add_u32_e32 v17, v17, v6
	s_waitcnt vmcnt(7)
	v_add_u32_e32 v17, v17, v7
	s_waitcnt vmcnt(6)
	v_add_u32_e32 v17, v17, v8
	s_waitcnt vmcnt(5)
	v_add_u32_e32 v17, v17, v9
	s_waitcnt vmcnt(4)
	v_add_u32_e32 v17, v17, v10
	s_waitcnt vmcnt(3)
	v_add_u32_e32 v17, v17, v11
	s_waitcnt vmcnt(2)
	v_add_u32_e32 v17, v17, v12
	s_waitcnt vmcnt(1)
	v_add_u32_e32 v17, v17, v13
	s_waitcnt vmcnt(0)
	v_add_u32_e32 v17, v17, v14
	v_cmp_eq_u32_e32 vcc, s2, v17
	s_cbranch_vccnz .LBB0_112
	s_and_b32 s33, s3, 0xff
	s_cmp_eq_u32 s33, 0
	s_mov_b64 s[48:49], -1
	s_sleep 3
	s_cbranch_scc0 .LBB0_117
	global_load_dword v17, v16, s[8:9] sc1
	s_waitcnt vmcnt(0)
	v_cmp_eq_u32_e32 vcc, 0, v17
	s_cbranch_vccnz .LBB0_119
	s_mov_b64 s[48:49], 0

.LBB0_129:
	s_and_b32 s3, s2, 0xff
	s_mov_b64 s[22:23], -1
	s_cmp_lg_u32 s3, 0
	s_mov_b64 s[26:27], -1
	s_sleep 3
	s_cbranch_scc1 .LBB0_132
	global_load_dword v2, v0, s[14:15] sc1
	s_waitcnt vmcnt(0)
	v_cmp_eq_u32_e32 vcc, 0, v2
	s_cbranch_vccnz .LBB0_134
	s_mov_b64 s[26:27], 0
	s_mov_b64 s[24:25], -1

.LBB0_146:
	s_and_b32 s3, s2, 0xff
	s_cmp_lg_u32 s3, 0
	s_mov_b64 s[22:23], -1
	s_sleep 3
	s_cbranch_scc1 .LBB0_149
	global_load_dword v1, v0, s[14:15] sc1
	s_waitcnt vmcnt(0)
	v_cmp_eq_u32_e32 vcc, 0, v1
	s_cbranch_vccnz .LBB0_151
	s_mov_b64 s[22:23], 0
	s_mov_b64 s[20:21], -1

; __device__ __forceinline__ unsigned xb_ld(unsigned* p)              { return __hip_atomic_load(p, __ATOMIC_RELAXED, __HIP_MEMORY_SCOPE_AGENT); }
; __device__ __forceinline__ void xcd_barrier_complete(unsigned* bar, unsigned x, unsigned& nloc, unsigned& nx) {
;     const unsigned G = gridDim.x * gridDim.y * gridDim.z;
;     unsigned sum, cnt, mine, sp = 0u;
;     for (;;) {
;         sum = 0u; cnt = 0u; mine = 0u;
; #pragma unroll
;         for (unsigned j = 0; j < 16; ++j) { const unsigned c = xb_ld(&bar[XB_XCNT(j)]); sum += c; cnt += (c > 0u) ? 1u : 0u; mine = (j == x) ? c : mine; }
;         if (sum == G) break;
;         __builtin_amdgcn_s_sleep(1);
;         if ((++sp & 255u) == 0u) { if (xb_ld(&bar[XB_TMO])) break; if (sp > XB_SPIN_CAP) { atomicAdd(&bar[XB_TMO], 1u); break; } }
;     }
.LBB0_205:
	global_load_dword v16, v0, s[34:35] sc1
	global_load_dword v1, v0, s[38:39] sc1
	global_load_dword v2, v0, s[40:41] sc1
	global_load_dword v3, v0, s[42:43] sc1
	global_load_dword v4, v0, s[44:45] sc1
	global_load_dword v5, v0, s[46:47] sc1
	global_load_dword v6, v0, s[48:49] sc1
	global_load_dword v7, v0, s[50:51] sc1
	global_load_dword v8, v0, s[52:53] sc1
	global_load_dword v9, v0, s[54:55] sc1
	global_load_dword v10, v0, s[56:57] sc1
	global_load_dword v11, v0, s[58:59] sc1
	global_load_dword v12, v0, s[62:63] sc1
	global_load_dword v13, v0, s[72:73] sc1
	global_load_dword v14, v0, s[80:81] sc1
	global_load_dword v15, v0, s[88:89] sc1
	s_mov_b64 s[90:91], -1
	s_mov_b64 s[96:97], -1
	s_waitcnt vmcnt(14)
	v_add_u32_e32 v17, v1, v16
	s_waitcnt vmcnt(13)
	v_add_u32_e32 v17, v17, v2
	s_waitcnt vmcnt(12)
	v_add_u32_e32 v17, v17, v3
	s_waitcnt vmcnt(11)
	v_add_u32_e32 v17, v17, v4
	s_waitcnt vmcnt(10)
	v_add_u32_e32 v17, v17, v5
	s_waitcnt vmcnt(9)
	v_add_u32_e32 v17, v17, v6
	s_waitcnt vmcnt(8)
	v_add_u32_e32 v17, v17, v7
	s_waitcnt vmcnt(7)
	v_add_u32_e32 v17, v17, v8
	s_waitcnt vmcnt(6)
	v_add_u32_e32 v17, v17, v9
	s_waitcnt vmcnt(5)
	v_add_u32_e32 v17, v17, v10
	s_waitcnt vmcnt(4)
	v_add_u32_e32 v17, v17, v11
	s_waitcnt vmcnt(3)
	v_add_u32_e32 v17, v17, v12
	s_waitcnt vmcnt(2)
	v_add_u32_e32 v17, v17, v13
	s_waitcnt vmcnt(1)
	v_add_u32_e32 v17, v17, v14
	s_waitcnt vmcnt(0)
	v_add_u32_e32 v17, v17, v15
	v_cmp_eq_u32_e32 vcc, s5, v17
	s_cbranch_vccnz .LBB0_204
	s_and_b32 s7, s6, 0xff
	s_cmp_eq_u32 s7, 0
	s_mov_b64 vcc, -1
	s_sleep 3
	s_cbranch_scc0 .LBB0_209
	global_load_dword v17, v0, s[26:27] sc1
	s_waitcnt vmcnt(0)
	v_cmp_eq_u32_e32 vcc, 0, v17
	s_cbranch_vccnz .LBB0_211
	s_mov_b64 vcc, 0

.LBB0_221:
	s_and_b32 s6, s5, 0xff
	s_mov_b64 s[48:49], -1
	s_cmp_lg_u32 s6, 0
	s_mov_b64 s[52:53], -1
	s_sleep 3
	s_cbranch_scc1 .LBB0_224
	global_load_dword v2, v0, s[40:41] sc1
	s_waitcnt vmcnt(0)
	v_cmp_eq_u32_e32 vcc, 0, v2
	s_cbranch_vccnz .LBB0_226
	s_mov_b64 s[52:53], 0
	s_mov_b64 s[50:51], -1

.LBB0_238:
	s_and_b32 s6, s5, 0xff
	s_mov_b64 s[46:47], -1
	s_cmp_lg_u32 s6, 0
	s_mov_b64 s[50:51], -1
	s_sleep 3
	s_cbranch_scc1 .LBB0_241
	global_load_dword v2, v0, s[40:41] sc1
	s_waitcnt vmcnt(0)
	v_cmp_eq_u32_e32 vcc, 0, v2
	s_cbranch_vccnz .LBB0_243
	s_mov_b64 s[50:51], 0
	s_mov_b64 s[48:49], -1

; __device__ __forceinline__ unsigned xb_ld(unsigned* p)              { return __hip_atomic_load(p, __ATOMIC_RELAXED, __HIP_MEMORY_SCOPE_AGENT); }
; __device__ __forceinline__ void xcd_barrier_complete(unsigned* bar, unsigned x, unsigned& nloc, unsigned& nx) {
;     const unsigned G = gridDim.x * gridDim.y * gridDim.z;
;     unsigned sum, cnt, mine, sp = 0u;
;     for (;;) {
;         sum = 0u; cnt = 0u; mine = 0u;
; #pragma unroll
;         for (unsigned j = 0; j < 16; ++j) { const unsigned c = xb_ld(&bar[XB_XCNT(j)]); sum += c; cnt += (c > 0u) ? 1u : 0u; mine = (j == x) ? c : mine; }
;         if (sum == G) break;
;         __builtin_amdgcn_s_sleep(1);
;         if ((++sp & 255u) == 0u) { if (xb_ld(&bar[XB_TMO])) break; if (sp > XB_SPIN_CAP) { atomicAdd(&bar[XB_TMO], 1u); break; } }
;     }
.LBB0_430:
	global_load_dword v16, v0, s[34:35] sc1
	global_load_dword v1, v0, s[38:39] sc1
	global_load_dword v2, v0, s[40:41] sc1
	global_load_dword v3, v0, s[42:43] sc1
	global_load_dword v4, v0, s[44:45] sc1
	global_load_dword v5, v0, s[46:47] sc1
	global_load_dword v6, v0, s[48:49] sc1
	global_load_dword v7, v0, s[50:51] sc1
	global_load_dword v8, v0, s[52:53] sc1
	global_load_dword v9, v0, s[54:55] sc1
	global_load_dword v10, v0, s[56:57] sc1
	global_load_dword v11, v0, s[58:59] sc1
	global_load_dword v12, v0, s[62:63] sc1
	global_load_dword v13, v0, s[72:73] sc1
	global_load_dword v14, v0, s[80:81] sc1
	global_load_dword v15, v0, s[88:89] sc1
	s_mov_b64 s[90:91], -1
	s_mov_b64 s[96:97], -1
	s_waitcnt vmcnt(14)
	v_add_u32_e32 v17, v1, v16
	s_waitcnt vmcnt(13)
	v_add_u32_e32 v17, v17, v2
	s_waitcnt vmcnt(12)
	v_add_u32_e32 v17, v17, v3
	s_waitcnt vmcnt(11)
	v_add_u32_e32 v17, v17, v4
	s_waitcnt vmcnt(10)
	v_add_u32_e32 v17, v17, v5
	s_waitcnt vmcnt(9)
	v_add_u32_e32 v17, v17, v6
	s_waitcnt vmcnt(8)
	v_add_u32_e32 v17, v17, v7
	s_waitcnt vmcnt(7)
	v_add_u32_e32 v17, v17, v8
	s_waitcnt vmcnt(6)
	v_add_u32_e32 v17, v17, v9
	s_waitcnt vmcnt(5)
	v_add_u32_e32 v17, v17, v10
	s_waitcnt vmcnt(4)
	v_add_u32_e32 v17, v17, v11
	s_waitcnt vmcnt(3)
	v_add_u32_e32 v17, v17, v12
	s_waitcnt vmcnt(2)
	v_add_u32_e32 v17, v17, v13
	s_waitcnt vmcnt(1)
	v_add_u32_e32 v17, v17, v14
	s_waitcnt vmcnt(0)
	v_add_u32_e32 v17, v17, v15
	v_cmp_eq_u32_e32 vcc, s4, v17
	s_cbranch_vccnz .LBB0_429
	s_and_b32 s6, s5, 0xff
	s_cmp_eq_u32 s6, 0
	s_mov_b64 vcc, -1
	s_sleep 3
	s_cbranch_scc0 .LBB0_434
	global_load_dword v17, v0, s[26:27] sc1
	s_waitcnt vmcnt(0)
	v_cmp_eq_u32_e32 vcc, 0, v17
	s_cbranch_vccnz .LBB0_436
	s_mov_b64 vcc, 0

.LBB0_446:
	s_and_b32 s5, s4, 0xff
	s_mov_b64 s[48:49], -1
	s_cmp_lg_u32 s5, 0
	s_mov_b64 s[52:53], -1
	s_sleep 3
	s_cbranch_scc1 .LBB0_449
	global_load_dword v2, v0, s[40:41] sc1
	s_waitcnt vmcnt(0)
	v_cmp_eq_u32_e32 vcc, 0, v2
	s_cbranch_vccnz .LBB0_451
	s_mov_b64 s[52:53], 0
	s_mov_b64 s[50:51], -1

.LBB0_463:
	s_and_b32 s5, s4, 0xff
	s_mov_b64 s[46:47], -1
	s_cmp_lg_u32 s5, 0
	s_mov_b64 s[50:51], -1
	s_sleep 3
	s_cbranch_scc1 .LBB0_466
	global_load_dword v2, v0, s[40:41] sc1
	s_waitcnt vmcnt(0)
	v_cmp_eq_u32_e32 vcc, 0, v2
	s_cbranch_vccnz .LBB0_468
	s_mov_b64 s[50:51], 0
	s_mov_b64 s[48:49], -1

; __device__ __forceinline__ unsigned xb_ld(unsigned* p)              { return __hip_atomic_load(p, __ATOMIC_RELAXED, __HIP_MEMORY_SCOPE_AGENT); }
; __device__ __forceinline__ void xcd_barrier_complete(unsigned* bar, unsigned x, unsigned& nloc, unsigned& nx) {
;     const unsigned G = gridDim.x * gridDim.y * gridDim.z;
;     unsigned sum, cnt, mine, sp = 0u;
;     for (;;) {
;         sum = 0u; cnt = 0u; mine = 0u;
; #pragma unroll
;         for (unsigned j = 0; j < 16; ++j) { const unsigned c = xb_ld(&bar[XB_XCNT(j)]); sum += c; cnt += (c > 0u) ? 1u : 0u; mine = (j == x) ? c : mine; }
;         if (sum == G) break;
;         __builtin_amdgcn_s_sleep(1);
;         if ((++sp & 255u) == 0u) { if (xb_ld(&bar[XB_TMO])) break; if (sp > XB_SPIN_CAP) { atomicAdd(&bar[XB_TMO], 1u); break; } }
;     }
.LBB0_1197:
	global_load_dword v16, v0, s[34:35] sc1
	global_load_dword v1, v0, s[38:39] sc1
	global_load_dword v2, v0, s[40:41] sc1
	global_load_dword v3, v0, s[42:43] sc1
	global_load_dword v4, v0, s[44:45] sc1
	global_load_dword v5, v0, s[46:47] sc1
	global_load_dword v6, v0, s[48:49] sc1
	global_load_dword v7, v0, s[50:51] sc1
	global_load_dword v8, v0, s[52:53] sc1
	global_load_dword v9, v0, s[54:55] sc1
	global_load_dword v10, v0, s[56:57] sc1
	global_load_dword v11, v0, s[58:59] sc1
	global_load_dword v12, v0, s[62:63] sc1
	global_load_dword v13, v0, s[72:73] sc1
	global_load_dword v14, v0, s[80:81] sc1
	global_load_dword v15, v0, s[86:87] sc1
	s_mov_b64 s[88:89], -1
	s_mov_b64 s[90:91], -1
	s_waitcnt vmcnt(14)
	v_add_u32_e32 v17, v1, v16
	s_waitcnt vmcnt(13)
	v_add_u32_e32 v17, v17, v2
	s_waitcnt vmcnt(12)
	v_add_u32_e32 v17, v17, v3
	s_waitcnt vmcnt(11)
	v_add_u32_e32 v17, v17, v4
	s_waitcnt vmcnt(10)
	v_add_u32_e32 v17, v17, v5
	s_waitcnt vmcnt(9)
	v_add_u32_e32 v17, v17, v6
	s_waitcnt vmcnt(8)
	v_add_u32_e32 v17, v17, v7
	s_waitcnt vmcnt(7)
	v_add_u32_e32 v17, v17, v8
	s_waitcnt vmcnt(6)
	v_add_u32_e32 v17, v17, v9
	s_waitcnt vmcnt(5)
	v_add_u32_e32 v17, v17, v10
	s_waitcnt vmcnt(4)
	v_add_u32_e32 v17, v17, v11
	s_waitcnt vmcnt(3)
	v_add_u32_e32 v17, v17, v12
	s_waitcnt vmcnt(2)
	v_add_u32_e32 v17, v17, v13
	s_waitcnt vmcnt(1)
	v_add_u32_e32 v17, v17, v14
	s_waitcnt vmcnt(0)
	v_add_u32_e32 v17, v17, v15
	v_cmp_eq_u32_e32 vcc, s5, v17
	s_cbranch_vccnz .LBB0_1196
	s_and_b32 s7, s6, 0xff
	s_cmp_eq_u32 s7, 0
	s_mov_b64 s[96:97], -1
	s_sleep 3
	s_cbranch_scc0 .LBB0_1201
	global_load_dword v17, v0, s[26:27] sc1
	s_waitcnt vmcnt(0)
	v_cmp_eq_u32_e32 vcc, 0, v17
	s_cbranch_vccnz .LBB0_1203
	s_mov_b64 s[96:97], 0

; __device__ __forceinline__ unsigned xb_ld(unsigned* p)              { return __hip_atomic_load(p, __ATOMIC_RELAXED, __HIP_MEMORY_SCOPE_AGENT); }
; __device__ __forceinline__ void xcd_barrier_complete(unsigned* bar, unsigned x, unsigned& nloc, unsigned& nx) {
;     const unsigned G = gridDim.x * gridDim.y * gridDim.z;
;     unsigned sum, cnt, mine, sp = 0u;
;     for (;;) {
;         sum = 0u; cnt = 0u; mine = 0u;
; #pragma unroll
;         for (unsigned j = 0; j < 16; ++j) { const unsigned c = xb_ld(&bar[XB_XCNT(j)]); sum += c; cnt += (c > 0u) ? 1u : 0u; mine = (j == x) ? c : mine; }
;         if (sum == G) break;
;         __builtin_amdgcn_s_sleep(1);
;         if ((++sp & 255u) == 0u) { if (xb_ld(&bar[XB_TMO])) break; if (sp > XB_SPIN_CAP) { atomicAdd(&bar[XB_TMO], 1u); break; } }
;     }
.LBB0_1399:
	global_load_dword v16, v0, s[34:35] sc1
	global_load_dword v1, v0, s[38:39] sc1
	global_load_dword v2, v0, s[40:41] sc1
	global_load_dword v3, v0, s[42:43] sc1
	global_load_dword v4, v0, s[44:45] sc1
	global_load_dword v5, v0, s[46:47] sc1
	global_load_dword v6, v0, s[48:49] sc1
	global_load_dword v7, v0, s[50:51] sc1
	global_load_dword v8, v0, s[52:53] sc1
	global_load_dword v9, v0, s[54:55] sc1
	global_load_dword v10, v0, s[56:57] sc1
	global_load_dword v11, v0, s[58:59] sc1
	global_load_dword v12, v0, s[62:63] sc1
	global_load_dword v13, v0, s[72:73] sc1
	global_load_dword v14, v0, s[80:81] sc1
	global_load_dword v15, v0, s[84:85] sc1
	s_mov_b64 s[86:87], -1
	s_mov_b64 s[88:89], -1
	s_waitcnt vmcnt(14)
	v_add_u32_e32 v17, v1, v16
	s_waitcnt vmcnt(13)
	v_add_u32_e32 v17, v17, v2
	s_waitcnt vmcnt(12)
	v_add_u32_e32 v17, v17, v3
	s_waitcnt vmcnt(11)
	v_add_u32_e32 v17, v17, v4
	s_waitcnt vmcnt(10)
	v_add_u32_e32 v17, v17, v5
	s_waitcnt vmcnt(9)
	v_add_u32_e32 v17, v17, v6
	s_waitcnt vmcnt(8)
	v_add_u32_e32 v17, v17, v7
	s_waitcnt vmcnt(7)
	v_add_u32_e32 v17, v17, v8
	s_waitcnt vmcnt(6)
	v_add_u32_e32 v17, v17, v9
	s_waitcnt vmcnt(5)
	v_add_u32_e32 v17, v17, v10
	s_waitcnt vmcnt(4)
	v_add_u32_e32 v17, v17, v11
	s_waitcnt vmcnt(3)
	v_add_u32_e32 v17, v17, v12
	s_waitcnt vmcnt(2)
	v_add_u32_e32 v17, v17, v13
	s_waitcnt vmcnt(1)
	v_add_u32_e32 v17, v17, v14
	s_waitcnt vmcnt(0)
	v_add_u32_e32 v17, v17, v15
	v_cmp_eq_u32_e32 vcc, s4, v17
	s_cbranch_vccnz .LBB0_1398
	s_and_b32 s6, s5, 0xff
	s_cmp_eq_u32 s6, 0
	s_mov_b64 s[90:91], -1
	s_sleep 3
	s_cbranch_scc0 .LBB0_1403
	global_load_dword v17, v0, s[26:27] sc1
	s_waitcnt vmcnt(0)
	v_cmp_eq_u32_e32 vcc, 0, v17
	s_cbranch_vccnz .LBB0_1405
	s_mov_b64 s[90:91], 0
